# row passes 0/1: next-row loads stay in flight (counted wait before register rotation, drain only on modulation reload); m0 save/restore removed around LDS-DMA; accumulator zero-init with v_mov_b64
# speedup vs baseline: 1.0067x; 1.0009x over previous
; template <int MODE, bool FIRSTX>
; __device__ __forceinline__ void row_pass(Frame& F, int layer, bool final_out, int row0) {
;     ...
;     if (r0 < r1) RP_LOAD(r0, xf, xb, yb);
;     int curm = -1;
;     for (int row = r0; row < r1; ++row) {
;         if (row + 1 < r1) RP_LOAD(row + 1, xfn, xbn, ybn);
;         const int mi = mod_index(row);
;         if (mi != curm) { curm = mi;
; #pragma unroll
;             for (int q = 0; q < 4; ++q) { const int c = RP_COL(q);
;                 if (MODE != 0) gt[q] = *(const f32x4*)(MOD + ((size_t)layer * 9 + mi) * 6144 + gate_i * 1024 + c);
;                 if (!final_out) { sh[q] = *(const f32x4*)(MOD + ((size_t)nlayer * 9 + mi) * 6144 + sh_i * 1024 + c); sc[q] = *(const f32x4*)(MOD + ((size_t)nlayer * 9 + mi) * 6144 + sc_i * 1024 + c); } } }
;         f32x4 v[4];
; #pragma unroll
;         for (int q = 0; q < 4; ++q) v[q] = FIRSTX ? xf[q] : RP_UNPK(xb[q >> 1], q & 1);
;         if (MODE != 0) {
; #pragma unroll
;             for (int q = 0; q < 4; ++q) { f32x4 y = (f32x4){0.f, 0.f, 0.f, 0.f};
; #pragma unroll
;                 for (int k = 0; k < NY; ++k) { if (MODE == 2) { const unsigned w8 = yb[k][q >> 1][q & 1]; const f32x2 lo = __builtin_amdgcn_cvt_pk_f32_fp8((int)w8, false), hi = __builtin_amdgcn_cvt_pk_f32_fp8((int)w8, true); y += (f32x4){lo.x, lo.y, hi.x, hi.y}; }
;                                                 else y += RP_UNPK(yb[k][q >> 1], q & 1); }
;                 if (MODE == 2) y = y * (1.0f / YK8_SCALE);
;                 v[q] = v[q] * DN_ALPHA + gt[q] * y; }
;             float s = 0.f;
; #pragma unroll
;             for (int q = 0; q < 4; ++q) s += (v[q][0] + v[q][1]) + (v[q][2] + v[q][3]);
;             const float mean = wave_sum(s) * (1.0f / DM); float qq = 0.f;
; #pragma unroll
;             for (int q = 0; q < 4; ++q) { v[q] = v[q] - mean; qq += (v[q][0] * v[q][0] + v[q][1] * v[q][1]) + (v[q][2] * v[q][2] + v[q][3] * v[q][3]); }
;             const float rstd = 1.0f / sqrtf(wave_sum(qq) * (1.0f / DM) + LN_EPS);
; #pragma unroll
;             for (int q = 0; q < 4; ++q) v[q] = v[q] * rstd * lg[q] + lb[q];
;             if (final_out) { if (row >= NCTX) {
; #pragma unroll
;                 for (int q = 0; q < 4; ++q) *(f32x4*)(F.out + (size_t)(row - NCTX) * DM + RP_COL(q)) = v[q]; } }
;             else {
; #pragma unroll
.LBB0_165:
	s_load_dwordx2 s[0:1], s[0:1], 0x0
	s_add_u32 s19, s94, 0x100000
	s_addc_u32 s20, s95, 0
	v_lshlrev_b32_e32 v0, 3, v0
	s_lshl_b64 s[4:5], s[4:5], 12
	v_and_b32_e32 v64, 0x1f8, v0
	s_waitcnt lgkmcnt(0)
	s_add_u32 s0, s0, s4
	s_addc_u32 s1, s1, s5
	v_lshlrev_b32_e32 v8, 2, v64
	global_load_dwordx4 v[0:3], v8, s[0:1] offset:2064
	global_load_dwordx4 v[4:7], v8, s[0:1] offset:2048
	global_load_dwordx4 v[12:15], v8, s[0:1] offset:16
	global_load_dwordx4 v[36:39], v8, s[0:1]
	s_lshl_b64 s[0:1], s[2:3], 10
	s_add_u32 s0, s94, s0
	v_mov_b32_e32 v65, 0
	s_addc_u32 s1, s95, s1
	v_or_b32_e32 v8, 0x200, v64
	v_lshl_add_u64 v[10:11], s[0:1], 0, v[64:65]
	s_mov_b64 s[0:1], 0x99000000
	s_add_i32 s3, s2, 1
	s_mov_b32 s5, 0
	v_lshl_add_u64 v[66:67], v[10:11], 0, s[0:1]
	s_ashr_i32 s21, s3, 31
	s_mov_b32 s22, -1
	s_mov_b64 s[6:7], 0
	v_lshlrev_b32_e32 v68, 2, v8
	s_mov_b64 s[10:11], 0x400
	v_mov_b32_e32 v24, v65
	v_mov_b32_e32 v25, v65
	v_mov_b32_e32 v26, v65
	v_mov_b32_e32 v27, v65
	v_mov_b32_e32 v20, v65
	v_mov_b32_e32 v21, v65
	v_mov_b32_e32 v22, v65
	v_mov_b32_e32 v23, v65
	v_mov_b32_e32 v44, v65
	v_mov_b32_e32 v45, v65
	v_mov_b32_e32 v46, v65
	v_mov_b32_e32 v47, v65
	v_mov_b32_e32 v40, v65
	v_mov_b32_e32 v41, v65
	v_mov_b32_e32 v42, v65
	v_mov_b32_e32 v43, v65
	s_branch .LBB0_167
.LBB0_166:
	s_waitcnt vmcnt(0)
.Lrp0_common:
	v_pk_add_f32 v[70:71], v[18:19], 1.0 op_sel_hi:[1,0]
	v_pk_add_f32 v[72:73], v[16:17], 1.0 op_sel_hi:[1,0]
	v_pk_fma_f32 v[38:39], v[38:39], v[70:71], v[26:27]
	v_pk_add_f32 v[70:71], v[8:9], 1.0 op_sel_hi:[1,0]
	v_pk_fma_f32 v[36:37], v[36:37], v[72:73], v[24:25]
	v_pk_fma_f32 v[12:13], v[12:13], v[70:71], v[20:21]
	v_mov_b32_e32 v71, 0
	v_cvt_pk_fp8_f32 v71, v12, v13
	v_pk_add_f32 v[12:13], v[10:11], 1.0 op_sel_hi:[1,0]
	v_mov_b32_e32 v70, 0
	v_pk_fma_f32 v[12:13], v[14:15], v[12:13], v[22:23]
	v_pk_add_f32 v[14:15], v[32:33], 1.0 op_sel_hi:[1,0]
	v_cvt_pk_fp8_f32 v71, v12, v13 op_sel:[0,0,1]
	v_pk_add_f32 v[12:13], v[34:35], 1.0 op_sel_hi:[1,0]
	v_cvt_pk_fp8_f32 v70, v36, v37
	v_pk_fma_f32 v[6:7], v[6:7], v[12:13], v[46:47]
	v_pk_add_f32 v[12:13], v[28:29], 1.0 op_sel_hi:[1,0]
	v_pk_fma_f32 v[4:5], v[4:5], v[14:15], v[44:45]
	v_pk_fma_f32 v[0:1], v[0:1], v[12:13], v[40:41]
	v_mov_b32_e32 v12, 0
	v_mov_b32_e32 v13, 0
	v_cvt_pk_fp8_f32 v12, v4, v5
	v_cvt_pk_fp8_f32 v13, v0, v1
	v_pk_add_f32 v[0:1], v[30:31], 1.0 op_sel_hi:[1,0]
	v_cvt_pk_fp8_f32 v70, v38, v39 op_sel:[0,0,1]
	v_pk_fma_f32 v[0:1], v[2:3], v[0:1], v[42:43]
	v_cvt_pk_fp8_f32 v12, v6, v7 op_sel:[0,0,1]
	v_cvt_pk_fp8_f32 v13, v0, v1 op_sel:[0,0,1]
	s_add_u32 s6, s6, 1
	global_store_dwordx2 v[66:67], v[70:71], off
	global_store_dwordx2 v[66:67], v[12:13], off offset:512
	s_addc_u32 s7, s7, 0
	s_add_i32 s0, s2, s6
	s_waitcnt vmcnt(2)
	v_mov_b64_e32 v[0:1], v[56:57]
	v_mov_b64_e32 v[4:5], v[60:61]
	v_mov_b64_e32 v[12:13], v[48:49]
	v_mov_b64_e32 v[36:37], v[52:53]
	v_lshl_add_u64 v[66:67], v[66:67], 0, s[10:11]
	s_cmp_lt_i32 s0, s18
	v_mov_b64_e32 v[2:3], v[58:59]
	v_mov_b64_e32 v[6:7], v[62:63]
	v_mov_b64_e32 v[14:15], v[50:51]
	v_mov_b64_e32 v[38:39], v[54:55]
	s_cbranch_scc0 .LBB0_177

; template <int MODE, bool FIRSTX>
; __device__ __forceinline__ void row_pass(Frame& F, int layer, bool final_out, int row0) {
;     ...
;     const int rpw = (TALL - row0 + F.NGW - 1) / F.NGW;
;     const int r0 = row0 + F.gw * rpw, r1 = (r0 + rpw < TALL) ? r0 + rpw : TALL;
;     const int sub = (MODE == 2) ? 1 : 0;
;     const int gate_i = (MODE == 2) ? 5 : 2;
;     const int nlayer = (MODE == 2) ? layer + 1 : layer;
;     const int sh_i = (MODE == 1) ? 3 : 0, sc_i = (MODE == 1) ? 4 : 1;
;     const int lc = 8 * F.lane;
;     ...
;     f32x4 lg[4], lb[4], gt[4], sh[4], sc[4];
;     if (MODE != 0) {
; #pragma unroll
;         for (int q = 0; q < 4; ++q) { lg[q] = *(const f32x4*)(INP(IN_LNG) + (layer * 2 + sub) * 1024 + RP_COL(q)); lb[q] = *(const f32x4*)(INP(IN_LNB) + (layer * 2 + sub) * 1024 + RP_COL(q)); } }
;     constexpr int NY = (MODE == 2) ? 4 : (MODE == 1 ? 1 : 0);
;     f32x4 xf[4], xfn[4]; u32x4 xb[2], xbn[2]; u32x4 yb[NY ? NY : 1][2], ybn[NY ? NY : 1][2];
;     ...
;     if (r0 < r1) RP_LOAD(r0, xf, xb, yb);
;     int curm = -1;
;     for (int row = r0; row < r1; ++row) {
;         if (row + 1 < r1) RP_LOAD(row + 1, xfn, xbn, ybn);
;         const int mi = mod_index(row);
;         if (mi != curm) { curm = mi;
; #pragma unroll
;             for (int q = 0; q < 4; ++q) { const int c = RP_COL(q);
;                 if (MODE != 0) gt[q] = *(const f32x4*)(MOD + ((size_t)layer * 9 + mi) * 6144 + gate_i * 1024 + c);
;                 if (!final_out) { sh[q] = *(const f32x4*)(MOD + ((size_t)nlayer * 9 + mi) * 6144 + sh_i * 1024 + c); sc[q] = *(const f32x4*)(MOD + ((size_t)nlayer * 9 + mi) * 6144 + sc_i * 1024 + c); } } }
;         f32x4 v[4];
; #pragma unroll
;         for (int q = 0; q < 4; ++q) v[q] = FIRSTX ? xf[q] : RP_UNPK(xb[q >> 1], q & 1);
;         if (MODE != 0) {
; #pragma unroll
;             for (int q = 0; q < 4; ++q) { f32x4 y = (f32x4){0.f, 0.f, 0.f, 0.f};
; #pragma unroll
;                 for (int k = 0; k < NY; ++k) { if (MODE == 2) { const unsigned w8 = yb[k][q >> 1][q & 1]; const f32x2 lo = __builtin_amdgcn_cvt_pk_f32_fp8((int)w8, false), hi = __builtin_amdgcn_cvt_pk_f32_fp8((int)w8, true); y += (f32x4){lo.x, lo.y, hi.x, hi.y}; }
;                                                 else y += RP_UNPK(yb[k][q >> 1], q & 1); }
;                 if (MODE == 2) y = y * (1.0f / YK8_SCALE);
;                 v[q] = v[q] * DN_ALPHA + gt[q] * y; }
.LBB0_750:
	s_or_b64 exec, exec, s[2:3]
	s_mov_b32 s0, s53
	s_mov_b32 s1, s73
	s_mov_b32 s2, s90
	s_waitcnt lgkmcnt(0)
	s_barrier
	v_mbcnt_lo_u32_b32 v132, -1, 0
	v_mbcnt_hi_u32_b32 v132, -1, v132
	s_lshl_b32 s8, s1, 3
	s_lshl_b32 s9, s2, 3
	s_add_i32 s8, s8, s0
	v_lshlrev_b32_e32 v0, 3, v132
	s_add_u32 s7, s74, 0x100000
	v_and_b32_e32 v134, 0x1f8, v0
	s_addc_u32 s10, s75, 0
	s_mov_b64 s[0:1], -1
	s_and_b64 vcc, exec, s[76:77]
	v_lshlrev_b32_e32 v136, 2, v134
	s_cbranch_vccz .LBB0_759
	s_add_i32 s0, s9, 0xffff
	s_sub_i32 s2, 0xffff0001, s9
	s_xor_b32 s1, s0, s9
	s_max_i32 s0, s0, s2
	s_abs_i32 s2, s9
	v_cvt_f32_u32_e32 v0, s2
	s_sub_i32 s3, 0, s2
	s_ashr_i32 s1, s1, 31
	v_rcp_iflag_f32_e32 v0, v0
	s_nop 0
	v_mul_f32_e32 v0, 0x4f7ffffe, v0
	v_cvt_u32_f32_e32 v0, v0
	s_nop 0
	v_readfirstlane_b32 s4, v0
	s_mul_i32 s3, s3, s4
	s_mul_hi_u32 s3, s4, s3
	s_add_i32 s4, s4, s3
	s_mul_hi_u32 s3, s0, s4
	s_mul_i32 s4, s3, s2
	s_sub_i32 s0, s0, s4
	s_add_i32 s4, s3, 1
	s_sub_i32 s5, s0, s2
	s_cmp_ge_u32 s0, s2
	s_cselect_b32 s3, s4, s3
	s_cselect_b32 s0, s5, s0
	s_add_i32 s4, s3, 1
	s_cmp_ge_u32 s0, s2
	s_cselect_b32 s0, s4, s3
	s_xor_b32 s0, s0, s1
	s_sub_i32 s0, s0, s1
	s_mul_i32 s11, s0, s8
	s_add_i32 s2, s11, 0x800
	s_add_i32 s3, s2, s0
	s_mov_b64 s[0:1], s[88:89]
	s_load_dwordx2 s[4:5], s[0:1], 0x30
	s_lshl_b32 s18, s37, 11
	s_lshl_b64 s[0:1], s[18:19], 2
	s_waitcnt lgkmcnt(0)
	s_add_u32 s4, s4, s0
	s_addc_u32 s5, s5, s1
	global_load_dwordx4 v[2:5], v136, s[4:5]
	s_mov_b64 s[4:5], s[88:89]
	s_load_dwordx2 s[4:5], s[4:5], 0x38
	s_waitcnt lgkmcnt(0)
	s_add_u32 s4, s4, s0
	s_addc_u32 s5, s5, s1
	global_load_dwordx4 v[6:9], v136, s[4:5]
	s_mov_b64 s[4:5], s[88:89]
	s_load_dwordx2 s[4:5], s[4:5], 0x30
	s_waitcnt lgkmcnt(0)
	s_add_u32 s4, s4, s0
	s_addc_u32 s5, s5, s1
	global_load_dwordx4 v[10:13], v136, s[4:5] offset:16
	s_mov_b64 s[4:5], s[88:89]
	s_load_dwordx2 s[4:5], s[4:5], 0x38
	s_waitcnt lgkmcnt(0)
	s_add_u32 s4, s4, s0
	s_addc_u32 s5, s5, s1
	global_load_dwordx4 v[14:17], v136, s[4:5] offset:16
	s_mov_b64 s[4:5], s[88:89]
	s_load_dwordx2 s[4:5], s[4:5], 0x30
	s_waitcnt lgkmcnt(0)
	s_add_u32 s4, s4, s0
	s_addc_u32 s5, s5, s1
	global_load_dwordx4 v[18:21], v136, s[4:5] offset:2048
	s_mov_b64 s[4:5], s[88:89]
	s_load_dwordx2 s[4:5], s[4:5], 0x38
	s_waitcnt lgkmcnt(0)
	s_add_u32 s4, s4, s0
	s_addc_u32 s5, s5, s1
	global_load_dwordx4 v[22:25], v136, s[4:5] offset:2048
	s_mov_b64 s[4:5], s[88:89]
	s_load_dwordx2 s[4:5], s[4:5], 0x30
	s_waitcnt lgkmcnt(0)
	s_add_u32 s4, s4, s0
	s_addc_u32 s5, s5, s1
	global_load_dwordx4 v[26:29], v136, s[4:5] offset:2064
	s_min_i32 s14, s3, 0x10800
	s_mov_b64 s[4:5], s[88:89]
	s_cmp_ge_i32 s2, s14
	s_cbranch_scc1 .LBB0_758
	s_load_dwordx2 s[4:5], s[4:5], 0x38
	v_lshlrev_b32_e32 v0, 1, v134
	s_waitcnt lgkmcnt(0)
	s_add_u32 s0, s4, s0
	s_addc_u32 s1, s5, s1
	s_ashr_i32 s3, s2, 31
	global_load_dwordx4 v[30:33], v136, s[0:1] offset:2064
	s_lshl_b64 s[0:1], s[2:3], 11
	s_add_u32 s4, s74, s0
	s_addc_u32 s5, s75, s1
	s_waitcnt vmcnt(11)
	v_lshl_add_u64 v[34:35], s[4:5], 0, v[0:1]
	s_mov_b64 s[4:5], 0x34400000
	s_waitcnt vmcnt(9)
	v_add_co_u32_e32 v38, vcc, s39, v34
	v_lshl_add_u64 v[36:37], v[34:35], 0, s[4:5]
	s_nop 0
	v_addc_co_u32_e32 v39, vcc, 0, v35, vcc
	s_mov_b64 s[4:5], 0x4d200000
	global_load_dwordx4 v[110:113], v[38:39], off
	global_load_dwordx4 v[106:109], v[36:37], off offset:1024
	v_lshl_add_u64 v[36:37], v[34:35], 0, s[4:5]
	s_mov_b32 s4, 0x4d200000
	v_add_co_u32_e32 v34, vcc, s4, v34
	v_mov_b32_e32 v115, s1
	s_nop 0
	v_addc_co_u32_e32 v35, vcc, 0, v35, vcc
	global_load_dwordx4 v[102:105], v[34:35], off
	global_load_dwordx4 v[98:101], v[36:37], off offset:1024
	v_lshlrev_b32_e32 v34, 4, v132
	v_and_b32_e32 v34, 0x3f0, v34
	v_or_b32_e32 v114, s0, v34
	s_lshl_b64 s[0:1], s[2:3], 10
	v_or_b32_e32 v116, s0, v134
	s_add_i32 s0, s11, 0x801
	v_mov_b32_e32 v117, s1
	s_ashr_i32 s1, s0, 31
	v_or_b32_e32 v0, 0x200, v134
	s_lshl_b64 s[0:1], s[0:1], 11
	v_or_b32_e32 v118, s0, v34
	v_mov_b32_e32 v119, s1
	s_mov_b32 s0, -1
	v_lshlrev_b32_e32 v0, 2, v0
	s_branch .LBB0_754
.LBB0_753:
	s_waitcnt vmcnt(0)
.Lrp1_common:
	v_lshlrev_b32_e32 v128, 16, v102
	v_and_b32_e32 v129, 0xffff0000, v102
	v_lshlrev_b32_e32 v102, 16, v103
	v_and_b32_e32 v103, 0xffff0000, v103
	v_pk_add_f32 v[102:103], v[102:103], 0 op_sel_hi:[1,0]
	v_pk_add_f32 v[128:129], v[128:129], 0 op_sel_hi:[1,0]
	v_lshlrev_b32_e32 v120, 16, v110
	v_and_b32_e32 v121, 0xffff0000, v110
	v_lshlrev_b32_e32 v110, 16, v111
	v_and_b32_e32 v111, 0xffff0000, v111
	v_pk_mul_f32 v[128:129], v[128:129], v[46:47]
	v_pk_mul_f32 v[102:103], v[102:103], v[48:49]
	v_lshlrev_b32_e32 v122, 16, v112
	v_pk_fma_f32 v[102:103], v[110:111], s[62:63], v[102:103] op_sel_hi:[1,0,1]
	v_pk_fma_f32 v[110:111], v[120:121], s[62:63], v[128:129] op_sel_hi:[1,0,1]
	v_lshlrev_b32_e32 v120, 16, v104
	v_and_b32_e32 v121, 0xffff0000, v104
	v_lshlrev_b32_e32 v104, 16, v105
	v_and_b32_e32 v105, 0xffff0000, v105
	v_pk_add_f32 v[104:105], v[104:105], 0 op_sel_hi:[1,0]
	v_pk_add_f32 v[120:121], v[120:121], 0 op_sel_hi:[1,0]
	v_and_b32_e32 v123, 0xffff0000, v112
	v_lshlrev_b32_e32 v112, 16, v113
	v_and_b32_e32 v113, 0xffff0000, v113
	v_pk_mul_f32 v[120:121], v[120:121], v[42:43]
	v_pk_mul_f32 v[104:105], v[104:105], v[44:45]
	v_lshlrev_b32_e32 v124, 16, v106
	v_pk_fma_f32 v[104:105], v[112:113], s[62:63], v[104:105] op_sel_hi:[1,0,1]
	v_pk_fma_f32 v[112:113], v[122:123], s[62:63], v[120:121] op_sel_hi:[1,0,1]
	v_lshlrev_b32_e32 v120, 16, v98
	v_and_b32_e32 v121, 0xffff0000, v98
	v_lshlrev_b32_e32 v98, 16, v99
	v_and_b32_e32 v99, 0xffff0000, v99
	v_pk_add_f32 v[98:99], v[98:99], 0 op_sel_hi:[1,0]
; template <int MODE, bool FIRSTX>
; __device__ __forceinline__ void row_pass(Frame& F, int layer, bool final_out, int row0) {
;     ...
;             float s = 0.f;
; #pragma unroll
;             for (int q = 0; q < 4; ++q) s += (v[q][0] + v[q][1]) + (v[q][2] + v[q][3]);
;             const float mean = wave_sum(s) * (1.0f / DM); float qq = 0.f;
; #pragma unroll
;             for (int q = 0; q < 4; ++q) { v[q] = v[q] - mean; qq += (v[q][0] * v[q][0] + v[q][1] * v[q][1]) + (v[q][2] * v[q][2] + v[q][3] * v[q][3]); }
;             const float rstd = 1.0f / sqrtf(wave_sum(qq) * (1.0f / DM) + LN_EPS);
; #pragma unroll
;             for (int q = 0; q < 4; ++q) v[q] = v[q] * rstd * lg[q] + lb[q];
	v_pk_add_f32 v[120:121], v[120:121], 0 op_sel_hi:[1,0]
	v_and_b32_e32 v125, 0xffff0000, v106
	v_lshlrev_b32_e32 v106, 16, v107
	v_and_b32_e32 v107, 0xffff0000, v107
	v_pk_mul_f32 v[120:121], v[120:121], v[78:79]
	v_pk_mul_f32 v[98:99], v[98:99], v[80:81]
	v_lshlrev_b32_e32 v126, 16, v108
	v_pk_fma_f32 v[98:99], v[106:107], s[62:63], v[98:99] op_sel_hi:[1,0,1]
	v_pk_fma_f32 v[106:107], v[124:125], s[62:63], v[120:121] op_sel_hi:[1,0,1]
	v_lshlrev_b32_e32 v120, 16, v100
	v_and_b32_e32 v121, 0xffff0000, v100
	v_lshlrev_b32_e32 v100, 16, v101
	v_and_b32_e32 v101, 0xffff0000, v101
	v_pk_add_f32 v[100:101], v[100:101], 0 op_sel_hi:[1,0]
	v_pk_add_f32 v[120:121], v[120:121], 0 op_sel_hi:[1,0]
	v_and_b32_e32 v127, 0xffff0000, v108
	v_lshlrev_b32_e32 v108, 16, v109
	v_and_b32_e32 v109, 0xffff0000, v109
	v_pk_mul_f32 v[120:121], v[120:121], v[70:71]
	v_pk_mul_f32 v[100:101], v[100:101], v[72:73]
	v_add_f32_e32 v122, v104, v105
	v_pk_fma_f32 v[100:101], v[108:109], s[62:63], v[100:101] op_sel_hi:[1,0,1]
	v_pk_fma_f32 v[108:109], v[126:127], s[62:63], v[120:121] op_sel_hi:[1,0,1]
	v_add_f32_e32 v120, v110, v111
	v_add_f32_e32 v121, v102, v103
	v_add_f32_e32 v120, v120, v121
	v_add_f32_e32 v121, v112, v113
	v_add_f32_e32 v120, 0, v120
	v_add_f32_e32 v121, v121, v122
	v_add_f32_e32 v120, v121, v120
	v_add_f32_e32 v121, v106, v107
	v_add_f32_e32 v122, v98, v99
	v_add_f32_e32 v121, v121, v122
	v_add_f32_e32 v120, v121, v120
	v_add_f32_e32 v121, v108, v109
	v_add_f32_e32 v122, v100, v101
	v_add_f32_e32 v121, v121, v122
	v_add_f32_e32 v120, v121, v120
	ds_swizzle_b32 v121, v120 offset:swizzle(SWAP,1)
	s_add_i32 s11, s11, 1
	v_lshl_add_u64 v[118:119], v[118:119], 0, s[50:51]
	s_cmp_lt_i32 s1, s14
	s_waitcnt lgkmcnt(0)
	v_add_f32_e32 v120, v120, v121
	ds_swizzle_b32 v121, v120 offset:swizzle(SWAP,2)
	s_waitcnt lgkmcnt(0)
	v_add_f32_e32 v120, v120, v121
	ds_swizzle_b32 v121, v120 offset:swizzle(SWAP,4)
	s_waitcnt lgkmcnt(0)
	v_add_f32_e32 v120, v120, v121
	ds_swizzle_b32 v121, v120 offset:swizzle(SWAP,8)
	s_waitcnt lgkmcnt(0)
	v_add_f32_e32 v120, v120, v121
	ds_swizzle_b32 v121, v120 offset:swizzle(SWAP,16)
	s_waitcnt lgkmcnt(0)
	v_add_f32_e32 v120, v120, v121
	v_mov_b32_e32 v121, v120
	s_nop 1
	v_permlane32_swap_b32_e32 v120, v121
	v_add_f32_e32 v120, v120, v121
	v_fmac_f32_e32 v103, 0xba800000, v120
	v_fmac_f32_e32 v111, 0xba800000, v120
	v_fmamk_f32 v102, v120, 0xba800000, v102
	v_fmamk_f32 v110, v120, 0xba800000, v110
	v_mul_f32_e32 v121, v111, v111
	v_mul_f32_e32 v122, v103, v103
	v_fmac_f32_e32 v121, v110, v110
	v_fmac_f32_e32 v122, v102, v102
	v_fmac_f32_e32 v105, 0xba800000, v120
	v_fmac_f32_e32 v113, 0xba800000, v120
	v_add_f32_e32 v121, v121, v122
	v_fmamk_f32 v104, v120, 0xba800000, v104
	v_fmamk_f32 v112, v120, 0xba800000, v112
	v_mul_f32_e32 v122, v113, v113
	v_mul_f32_e32 v123, v105, v105
	v_fmac_f32_e32 v122, v112, v112
	v_fmac_f32_e32 v123, v104, v104
	v_add_f32_e32 v122, v122, v123
	v_fmac_f32_e32 v99, 0xba800000, v120
	v_fmac_f32_e32 v107, 0xba800000, v120
	v_add_f32_e32 v121, v121, v122
	v_fmamk_f32 v98, v120, 0xba800000, v98
	v_fmamk_f32 v106, v120, 0xba800000, v106
	v_mul_f32_e32 v122, v107, v107
	v_mul_f32_e32 v123, v99, v99
	v_fmac_f32_e32 v122, v106, v106
	v_fmac_f32_e32 v123, v98, v98
	v_add_f32_e32 v122, v122, v123
	v_fmac_f32_e32 v101, 0xba800000, v120
	v_fmac_f32_e32 v109, 0xba800000, v120
	v_add_f32_e32 v121, v122, v121
	v_fmamk_f32 v100, v120, 0xba800000, v100
	v_fmamk_f32 v108, v120, 0xba800000, v108
	v_mul_f32_e32 v120, v109, v109
	v_mul_f32_e32 v122, v101, v101
	v_fmac_f32_e32 v120, v108, v108
	v_fmac_f32_e32 v122, v100, v100
	v_add_f32_e32 v120, v120, v122
	v_add_f32_e32 v120, v120, v121
	ds_swizzle_b32 v121, v120 offset:swizzle(SWAP,1)
	s_waitcnt lgkmcnt(0)
	v_add_f32_e32 v120, v120, v121
	ds_swizzle_b32 v121, v120 offset:swizzle(SWAP,2)
	s_waitcnt lgkmcnt(0)
	v_add_f32_e32 v120, v120, v121
	ds_swizzle_b32 v121, v120 offset:swizzle(SWAP,4)
	s_waitcnt lgkmcnt(0)
	v_add_f32_e32 v120, v120, v121
	ds_swizzle_b32 v121, v120 offset:swizzle(SWAP,8)
	s_waitcnt lgkmcnt(0)
	v_add_f32_e32 v120, v120, v121
	ds_swizzle_b32 v121, v120 offset:swizzle(SWAP,16)
	s_waitcnt lgkmcnt(0)
	v_add_f32_e32 v120, v120, v121
	v_mov_b32_e32 v121, v120
	s_nop 1
	v_permlane32_swap_b32_e32 v120, v121
	v_add_f32_e32 v120, v120, v121
	v_fmamk_f32 v120, v120, 0x3a800000, v188
	v_mul_f32_e32 v121, 0x4f800000, v120
	v_cmp_gt_f32_e32 vcc, s31, v120
	s_nop 1
	v_cndmask_b32_e32 v120, v120, v121, vcc
	v_sqrt_f32_e32 v121, v120
	s_nop 0
	v_add_u32_e32 v122, -1, v121
	v_fma_f32 v123, -v122, v121, v120
	v_cmp_ge_f32_e64 s[2:3], 0, v123
	v_add_u32_e32 v123, 1, v121
	s_nop 0
	v_cndmask_b32_e64 v122, v121, v122, s[2:3]
	v_fma_f32 v121, -v123, v121, v120
	v_cmp_lt_f32_e64 s[2:3], 0, v121
	s_nop 1
	v_cndmask_b32_e64 v121, v122, v123, s[2:3]
	v_mul_f32_e32 v122, 0x37800000, v121
	v_cndmask_b32_e32 v121, v121, v122, vcc
	v_cmp_class_f32_e32 vcc, v120, v189
	s_nop 1
	v_cndmask_b32_e32 v120, v121, v120, vcc
	v_div_scale_f32 v121, s[2:3], v120, v120, 1.0
	v_rcp_f32_e32 v122, v121
	s_nop 0
	v_fma_f32 v123, -v121, v122, 1.0
	v_fmac_f32_e32 v122, v123, v122
	v_div_scale_f32 v123, vcc, 1.0, v120, 1.0
	v_mul_f32_e32 v124, v123, v122
	v_fma_f32 v125, -v121, v124, v123
	v_fmac_f32_e32 v124, v125, v122
	v_fma_f32 v121, -v121, v124, v123
	v_div_fmas_f32 v121, v121, v122, v124
	v_div_fixup_f32 v120, v121, v120, 1.0
	v_pk_mul_f32 v[110:111], v[110:111], v[120:121] op_sel_hi:[1,0]
	v_pk_mul_f32 v[98:99], v[98:99], v[120:121] op_sel_hi:[1,0]
	v_pk_fma_f32 v[110:111], v[2:3], v[110:111], v[6:7]
	v_pk_fma_f32 v[122:123], v[20:21], v[98:99], v[24:25]
	v_pk_mul_f32 v[98:99], v[100:101], v[120:121] op_sel_hi:[1,0]
; __device__ __forceinline__ unsigned pk2(float lo, float hi) { return f2bf(lo) | (f2bf(hi) << 16); }
; template <int MODE, bool FIRSTX>
; __device__ __forceinline__ void row_pass(Frame& F, int layer, bool final_out, int row0) {
;     ...
;             for (int q = 0; q < 4; ++q) v[q] = v[q] * rstd * lg[q] + lb[q];
;             if (final_out) { if (row >= NCTX) {
; #pragma unroll
;                 for (int q = 0; q < 4; ++q) *(f32x4*)(F.out + (size_t)(row - NCTX) * DM + RP_COL(q)) = v[q]; } }
;             else {
; #pragma unroll
;                 for (int j = 0; j < 2; ++j) { u32x4 w; w.x = pk2(v[2 * j][0], v[2 * j][1]); w.y = pk2(v[2 * j][2], v[2 * j][3]); w.z = pk2(v[2 * j + 1][0], v[2 * j + 1][1]); w.w = pk2(v[2 * j + 1][2], v[2 * j + 1][3]);
;                     *(u32x4*)(X + (size_t)row * DM + lc + 512 * j) = w; } }
;         }
;         if (!final_out) {
; #pragma unroll
;             for (int j = 0; j < 2; ++j) { const f32x4 h0 = v[2 * j] * (sc[2 * j] + 1.0f) + sh[2 * j], h1 = v[2 * j + 1] * (sc[2 * j + 1] + 1.0f) + sh[2 * j + 1];
;                 if (MODE == 1 || (nlayer % 3) == 2) { u32x4 w; w.x = pk2(h0[0], h0[1]); w.y = pk2(h0[2], h0[3]); w.z = pk2(h1[0], h1[1]); w.w = pk2(h1[2], h1[3]);
;                     *(u32x4*)(H + (size_t)row * DM + lc + 512 * j) = w; }
	v_pk_mul_f32 v[102:103], v[102:103], v[120:121] op_sel_hi:[1,0]
	v_pk_mul_f32 v[112:113], v[112:113], v[120:121] op_sel_hi:[1,0]
	v_pk_mul_f32 v[104:105], v[104:105], v[120:121] op_sel_hi:[1,0]
	v_pk_mul_f32 v[106:107], v[106:107], v[120:121] op_sel_hi:[1,0]
	v_pk_mul_f32 v[100:101], v[108:109], v[120:121] op_sel_hi:[1,0]
	v_pk_fma_f32 v[120:121], v[28:29], v[98:99], v[32:33]
	v_bfe_u32 v98, v110, 16, 1
	v_add3_u32 v98, v110, v98, s43
	v_bfe_u32 v99, v111, 16, 1
	v_pk_fma_f32 v[102:103], v[4:5], v[102:103], v[8:9]
	v_lshrrev_b32_e32 v98, 16, v98
	v_add3_u32 v99, v111, v99, s43
	v_and_or_b32 v98, v99, s33, v98
	v_bfe_u32 v99, v102, 16, 1
	v_pk_fma_f32 v[108:109], v[26:27], v[100:101], v[30:31]
	v_add3_u32 v99, v102, v99, s43
	v_bfe_u32 v100, v103, 16, 1
	v_pk_fma_f32 v[112:113], v[10:11], v[112:113], v[14:15]
	v_lshrrev_b32_e32 v99, 16, v99
	v_add3_u32 v100, v103, v100, s43
	v_and_or_b32 v99, v100, s33, v99
	v_bfe_u32 v100, v112, 16, 1
	v_add3_u32 v100, v112, v100, s43
	v_bfe_u32 v101, v113, 16, 1
	v_pk_fma_f32 v[104:105], v[12:13], v[104:105], v[16:17]
	v_lshrrev_b32_e32 v100, 16, v100
	v_add3_u32 v101, v113, v101, s43
	v_and_or_b32 v100, v101, s33, v100
	v_bfe_u32 v101, v104, 16, 1
	v_add3_u32 v101, v104, v101, s43
	v_bfe_u32 v126, v105, 16, 1
	v_lshl_add_u64 v[124:125], s[74:75], 0, v[114:115]
	v_lshrrev_b32_e32 v101, 16, v101
	v_add3_u32 v126, v105, v126, s43
	v_and_or_b32 v101, v126, s33, v101
	v_add_co_u32_e32 v126, vcc, s39, v124
	v_pk_fma_f32 v[106:107], v[18:19], v[106:107], v[22:23]
	s_nop 0
	v_addc_co_u32_e32 v127, vcc, 0, v125, vcc
	global_store_dwordx4 v[126:127], v[98:101], off
	v_bfe_u32 v128, v121, 16, 1
	v_add3_u32 v128, v121, v128, s43
	v_bfe_u32 v98, v106, 16, 1
	v_add3_u32 v98, v106, v98, s43
	v_bfe_u32 v99, v107, 16, 1
	v_lshrrev_b32_e32 v98, 16, v98
	v_add3_u32 v99, v107, v99, s43
	v_and_or_b32 v98, v99, s33, v98
	v_bfe_u32 v99, v122, 16, 1
	v_add3_u32 v99, v122, v99, s43
	v_bfe_u32 v100, v123, 16, 1
	v_lshrrev_b32_e32 v99, 16, v99
	v_add3_u32 v100, v123, v100, s43
	v_and_or_b32 v99, v100, s33, v99
	v_bfe_u32 v100, v108, 16, 1
	v_add3_u32 v100, v108, v100, s43
	v_bfe_u32 v101, v109, 16, 1
	v_lshrrev_b32_e32 v100, 16, v100
	v_add3_u32 v101, v109, v101, s43
	v_and_or_b32 v100, v101, s33, v100
	v_bfe_u32 v101, v120, 16, 1
	v_add3_u32 v101, v120, v101, s43
	v_lshrrev_b32_e32 v101, 16, v101
	v_and_or_b32 v101, v128, s33, v101
	global_store_dwordx4 v[126:127], v[98:101], off offset:1024
	v_lshl_add_u64 v[114:115], v[114:115], 0, s[50:51]
	s_nop 0
	v_pk_add_f32 v[98:99], v[76:77], 1.0 op_sel_hi:[1,0]
	v_pk_add_f32 v[100:101], v[74:75], 1.0 op_sel_hi:[1,0]
	v_pk_fma_f32 v[102:103], v[98:99], v[102:103], v[64:65]
	v_pk_fma_f32 v[110:111], v[100:101], v[110:111], v[62:63]
	v_pk_add_f32 v[98:99], v[68:69], 1.0 op_sel_hi:[1,0]
	v_pk_add_f32 v[100:101], v[66:67], 1.0 op_sel_hi:[1,0]
	v_pk_fma_f32 v[104:105], v[98:99], v[104:105], v[60:61]
	v_and_b32_sdwa v99, v110, v185 dst_sel:DWORD dst_unused:UNUSED_PAD src0_sel:WORD_1 src1_sel:DWORD
	v_pk_fma_f32 v[112:113], v[100:101], v[112:113], v[58:59]
	v_add3_u32 v100, v110, v99, s43
	v_and_b32_sdwa v99, v103, v185 dst_sel:DWORD dst_unused:UNUSED_PAD src0_sel:WORD_1 src1_sel:DWORD
	v_and_b32_sdwa v101, v111, v185 dst_sel:DWORD dst_unused:UNUSED_PAD src0_sel:WORD_1 src1_sel:DWORD
	v_and_b32_sdwa v98, v102, v185 dst_sel:DWORD dst_unused:UNUSED_PAD src0_sel:WORD_1 src1_sel:DWORD
	v_add3_u32 v99, v103, v99, s43
	v_add3_u32 v101, v111, v101, s43
	v_add3_u32 v98, v102, v98, s43
	v_and_b32_e32 v99, 0xffff0000, v99
	v_and_b32_e32 v101, 0xffff0000, v101
	v_or_b32_sdwa v99, v99, v98 dst_sel:DWORD dst_unused:UNUSED_PAD src0_sel:DWORD src1_sel:WORD_1
	v_or_b32_sdwa v98, v101, v100 dst_sel:DWORD dst_unused:UNUSED_PAD src0_sel:DWORD src1_sel:WORD_1
	v_and_b32_sdwa v101, v112, v185 dst_sel:DWORD dst_unused:UNUSED_PAD src0_sel:WORD_1 src1_sel:DWORD
	v_add3_u32 v126, v112, v101, s43
	v_and_b32_sdwa v101, v105, v185 dst_sel:DWORD dst_unused:UNUSED_PAD src0_sel:WORD_1 src1_sel:DWORD
; __device__ __forceinline__ unsigned pk2(float lo, float hi) { return f2bf(lo) | (f2bf(hi) << 16); }
; __device__ __forceinline__ unsigned cvt_fp8x4(float a, float b, float c, float d) { int w = __builtin_amdgcn_cvt_pk_fp8_f32(a, b, 0, false); w = __builtin_amdgcn_cvt_pk_fp8_f32(c, d, w, true); return (unsigned)w; }
; template <int MODE, bool FIRSTX>
; __device__ __forceinline__ void row_pass(Frame& F, int layer, bool final_out, int row0) {
;     ...
;             for (int j = 0; j < 2; ++j) { const f32x4 h0 = v[2 * j] * (sc[2 * j] + 1.0f) + sh[2 * j], h1 = v[2 * j + 1] * (sc[2 * j + 1] + 1.0f) + sh[2 * j + 1];
;                 if (MODE == 1 || (nlayer % 3) == 2) { u32x4 w; w.x = pk2(h0[0], h0[1]); w.y = pk2(h0[2], h0[3]); w.z = pk2(h1[0], h1[1]); w.w = pk2(h1[2], h1[3]);
;                     *(u32x4*)(H + (size_t)row * DM + lc + 512 * j) = w; }
;                 if (MODE == 1 || (nlayer % 3) != 2) {                                u32x2 w8; w8.x = cvt_fp8x4(h0[0], h0[1], h0[2], h0[3]); w8.y = cvt_fp8x4(h1[0], h1[1], h1[2], h1[3]); *(u32x2*)(F.ws + WS_H8 + (size_t)row * DM + lc + 512 * j) = w8; } }
;         }
; #pragma unroll
;         for (int q = 0; q < 4; ++q) xf[q] = xfn[q];
; #pragma unroll
;         for (int j = 0; j < 2; ++j) { xb[j] = xbn[j];
; #pragma unroll
;             for (int k = 0; k < (NY ? NY : 1); ++k) yb[k][j] = ybn[k][j]; }
	v_and_b32_sdwa v127, v113, v185 dst_sel:DWORD dst_unused:UNUSED_PAD src0_sel:WORD_1 src1_sel:DWORD
	v_and_b32_sdwa v100, v104, v185 dst_sel:DWORD dst_unused:UNUSED_PAD src0_sel:WORD_1 src1_sel:DWORD
	v_add3_u32 v101, v105, v101, s43
	v_add3_u32 v127, v113, v127, s43
	v_add3_u32 v100, v104, v100, s43
	v_and_b32_e32 v101, 0xffff0000, v101
	v_and_b32_e32 v127, 0xffff0000, v127
	v_or_b32_sdwa v101, v101, v100 dst_sel:DWORD dst_unused:UNUSED_PAD src0_sel:DWORD src1_sel:WORD_1
	v_or_b32_sdwa v100, v127, v126 dst_sel:DWORD dst_unused:UNUSED_PAD src0_sel:DWORD src1_sel:WORD_1
	v_mov_b32_e32 v126, v1
	v_cvt_pk_fp8_f32 v126, v110, v111
	v_mov_b32_e32 v127, v1
	v_add_co_u32_e32 v110, vcc, s28, v124
	v_cvt_pk_fp8_f32 v127, v112, v113
	s_nop 0
	v_addc_co_u32_e32 v111, vcc, 0, v125, vcc
	global_store_dwordx4 v[110:111], v[98:101], off
	v_cvt_pk_fp8_f32 v126, v102, v103 op_sel:[0,0,1]
	v_cvt_pk_fp8_f32 v127, v104, v105 op_sel:[0,0,1]
	v_lshl_add_u64 v[98:99], s[74:75], 0, v[116:117]
	v_add_co_u32_e32 v102, vcc, s38, v98
	v_pk_add_f32 v[100:101], v[94:95], 1.0 op_sel_hi:[1,0]
	s_nop 0
	v_addc_co_u32_e32 v103, vcc, 0, v99, vcc
	v_pk_add_f32 v[98:99], v[96:97], 1.0 op_sel_hi:[1,0]
	v_pk_fma_f32 v[100:101], v[100:101], v[106:107], v[86:87]
	v_pk_fma_f32 v[104:105], v[98:99], v[122:123], v[88:89]
	v_pk_add_f32 v[98:99], v[92:93], 1.0 op_sel_hi:[1,0]
	v_pk_add_f32 v[106:107], v[90:91], 1.0 op_sel_hi:[1,0]
	v_pk_fma_f32 v[112:113], v[98:99], v[120:121], v[84:85]
	v_and_b32_sdwa v99, v100, v185 dst_sel:DWORD dst_unused:UNUSED_PAD src0_sel:WORD_1 src1_sel:DWORD
	v_pk_fma_f32 v[106:107], v[106:107], v[108:109], v[82:83]
	v_add3_u32 v108, v100, v99, s43
	v_and_b32_sdwa v99, v105, v185 dst_sel:DWORD dst_unused:UNUSED_PAD src0_sel:WORD_1 src1_sel:DWORD
	v_and_b32_sdwa v109, v101, v185 dst_sel:DWORD dst_unused:UNUSED_PAD src0_sel:WORD_1 src1_sel:DWORD
	v_and_b32_sdwa v98, v104, v185 dst_sel:DWORD dst_unused:UNUSED_PAD src0_sel:WORD_1 src1_sel:DWORD
	v_add3_u32 v99, v105, v99, s43
	v_add3_u32 v109, v101, v109, s43
	v_add3_u32 v98, v104, v98, s43
	v_and_b32_e32 v99, 0xffff0000, v99
	v_and_b32_e32 v109, 0xffff0000, v109
	v_or_b32_sdwa v99, v99, v98 dst_sel:DWORD dst_unused:UNUSED_PAD src0_sel:DWORD src1_sel:WORD_1
	v_or_b32_sdwa v98, v109, v108 dst_sel:DWORD dst_unused:UNUSED_PAD src0_sel:DWORD src1_sel:WORD_1
	v_and_b32_sdwa v108, v112, v185 dst_sel:DWORD dst_unused:UNUSED_PAD src0_sel:WORD_1 src1_sel:DWORD
	v_and_b32_sdwa v109, v106, v185 dst_sel:DWORD dst_unused:UNUSED_PAD src0_sel:WORD_1 src1_sel:DWORD
	v_add3_u32 v120, v106, v109, s43
	v_add3_u32 v121, v112, v108, s43
	v_and_b32_sdwa v108, v113, v185 dst_sel:DWORD dst_unused:UNUSED_PAD src0_sel:WORD_1 src1_sel:DWORD
	v_and_b32_sdwa v109, v107, v185 dst_sel:DWORD dst_unused:UNUSED_PAD src0_sel:WORD_1 src1_sel:DWORD
	v_add3_u32 v122, v113, v108, s43
	v_add3_u32 v123, v107, v109, s43
	v_mov_b32_e32 v108, v1
	v_mov_b32_e32 v109, v1
	v_cvt_pk_fp8_f32 v108, v100, v101
	v_cvt_pk_fp8_f32 v109, v106, v107
	v_and_b32_e32 v100, 0xffff0000, v122
	v_and_b32_e32 v106, 0xffff0000, v123
	v_cvt_pk_fp8_f32 v108, v104, v105 op_sel:[0,0,1]
	v_cvt_pk_fp8_f32 v109, v112, v113 op_sel:[0,0,1]
	v_or_b32_sdwa v101, v100, v121 dst_sel:DWORD dst_unused:UNUSED_PAD src0_sel:DWORD src1_sel:WORD_1
	v_or_b32_sdwa v100, v106, v120 dst_sel:DWORD dst_unused:UNUSED_PAD src0_sel:DWORD src1_sel:WORD_1
	global_store_dwordx2 v[102:103], v[126:127], off
	global_store_dwordx4 v[110:111], v[98:101], off offset:1024
	global_store_dwordx2 v[102:103], v[108:109], off offset:512
	v_lshl_add_u64 v[116:117], v[116:117], 0, s[54:55]
	s_waitcnt vmcnt(6)
	v_mov_b32_e32 v102, v54
	v_mov_b32_e32 v103, v55
	v_mov_b32_e32 v104, v56
	v_mov_b32_e32 v105, v57
	v_mov_b32_e32 v98, v50
	v_mov_b32_e32 v99, v51
	v_mov_b32_e32 v100, v52
	v_mov_b32_e32 v101, v53
	v_mov_b32_e32 v110, v38
	v_mov_b32_e32 v111, v39
	v_mov_b32_e32 v112, v40
	v_mov_b32_e32 v113, v41
	v_mov_b32_e32 v106, v34
	v_mov_b32_e32 v107, v35
	v_mov_b32_e32 v108, v36
	v_mov_b32_e32 v109, v37
	s_cbranch_scc0 .LBB0_758

; #define RP_UNPK(V_, H_) ((H_) ? (f32x4){bflo((V_)[2]), bfhi((V_)[2]), bflo((V_)[3]), bfhi((V_)[3])} : (f32x4){bflo((V_)[0]), bfhi((V_)[0]), bflo((V_)[1]), bfhi((V_)[1])})
; template <int MODE, bool FIRSTX>
; __device__ __forceinline__ void row_pass(Frame& F, int layer, bool final_out, int row0) {
;     ...
;     if (r0 < r1) RP_LOAD(r0, xf, xb, yb);
;     int curm = -1;
;     for (int row = r0; row < r1; ++row) {
;         if (row + 1 < r1) RP_LOAD(row + 1, xfn, xbn, ybn);
;         const int mi = mod_index(row);
;         if (mi != curm) { curm = mi;
; #pragma unroll
;             for (int q = 0; q < 4; ++q) { const int c = RP_COL(q);
;                 if (MODE != 0) gt[q] = *(const f32x4*)(MOD + ((size_t)layer * 9 + mi) * 6144 + gate_i * 1024 + c);
;                 if (!final_out) { sh[q] = *(const f32x4*)(MOD + ((size_t)nlayer * 9 + mi) * 6144 + sh_i * 1024 + c); sc[q] = *(const f32x4*)(MOD + ((size_t)nlayer * 9 + mi) * 6144 + sc_i * 1024 + c); } } }
;         f32x4 v[4];
; #pragma unroll
;         for (int q = 0; q < 4; ++q) v[q] = FIRSTX ? xf[q] : RP_UNPK(xb[q >> 1], q & 1);
;         if (MODE != 0) {
; #pragma unroll
;             for (int q = 0; q < 4; ++q) { f32x4 y = (f32x4){0.f, 0.f, 0.f, 0.f};
; #pragma unroll
;                 for (int k = 0; k < NY; ++k) { if (MODE == 2) { const unsigned w8 = yb[k][q >> 1][q & 1]; const f32x2 lo = __builtin_amdgcn_cvt_pk_f32_fp8((int)w8, false), hi = __builtin_amdgcn_cvt_pk_f32_fp8((int)w8, true); y += (f32x4){lo.x, lo.y, hi.x, hi.y}; }
;                                                 else y += RP_UNPK(yb[k][q >> 1], q & 1); }
;                 if (MODE == 2) y = y * (1.0f / YK8_SCALE);
;                 v[q] = v[q] * DN_ALPHA + gt[q] * y; }
;             float s = 0.f;
; #pragma unroll
;             for (int q = 0; q < 4; ++q) s += (v[q][0] + v[q][1]) + (v[q][2] + v[q][3]);
;             const float mean = wave_sum(s) * (1.0f / DM); float qq = 0.f;
; #pragma unroll
;             for (int q = 0; q < 4; ++q) { v[q] = v[q] - mean; qq += (v[q][0] * v[q][0] + v[q][1] * v[q][1]) + (v[q][2] * v[q][2] + v[q][3] * v[q][3]); }
;             const float rstd = 1.0f / sqrtf(wave_sum(qq) * (1.0f / DM) + LN_EPS);
.LBB0_765:
	s_add_u32 s14, s74, 0x4d200000
	s_addc_u32 s15, s75, 0
	s_lshl_b64 s[8:9], s[8:9], 11
	s_add_u32 s8, s14, s8
	s_addc_u32 s9, s15, s9
	v_lshlrev_b32_e32 v0, 1, v134
	global_load_dwordx4 v[122:125], v0, s[8:9]
	global_load_dwordx4 v[114:117], v0, s[8:9] offset:1024
	global_load_dwordx4 v[106:109], v136, s[2:3] offset:2064
	global_load_dwordx4 v[110:113], v136, s[2:3] offset:2048
	global_load_dwordx4 v[118:121], v136, s[2:3] offset:16
	global_load_dwordx4 v[126:129], v136, s[2:3]
	s_add_i32 s26, s18, 1
	s_waitcnt vmcnt(17)
	v_or_b32_e32 v34, 0x200, v134
	v_lshl_add_u64 v[130:131], s[14:15], 0, v[0:1]
	s_lshl_b64 s[2:3], s[0:1], 11
	v_and_b32_e32 v0, 63, v132
	s_lshl_b64 s[0:1], s[0:1], 10
	s_ashr_i32 s27, s26, 31
	v_lshl_or_b32 v132, v0, 4, s2
	v_mov_b32_e32 v133, s3
	v_mov_b32_e32 v135, s1
	v_or_b32_e32 v134, s0, v134
	s_lshl_b64 s[60:61], s[26:27], 12
	s_mov_b32 s5, -1
	s_mov_b64 s[76:77], 0
	v_lshlrev_b32_e32 v0, 2, v34
	s_branch .LBB0_767
.LBB0_766:
	s_waitcnt vmcnt(0)
.Lrp1f_common:
	v_lshlrev_b32_e32 v138, 16, v122
	v_and_b32_e32 v139, 0xffff0000, v122
	v_lshlrev_b32_e32 v122, 16, v123
	v_and_b32_e32 v123, 0xffff0000, v123
	v_pk_add_f32 v[122:123], v[122:123], 0 op_sel_hi:[1,0]
	v_pk_add_f32 v[138:139], v[138:139], 0 op_sel_hi:[1,0]
	v_pk_mul_f32 v[122:123], v[122:123], v[40:41]
	v_pk_mul_f32 v[138:139], v[138:139], v[38:39]
	v_pk_fma_f32 v[122:123], v[128:129], s[62:63], v[122:123] op_sel_hi:[1,0,1]
	v_lshlrev_b32_e32 v128, 16, v124
	v_and_b32_e32 v129, 0xffff0000, v124
	v_lshlrev_b32_e32 v124, 16, v125
	v_and_b32_e32 v125, 0xffff0000, v125
	v_pk_add_f32 v[124:125], v[124:125], 0 op_sel_hi:[1,0]
	v_pk_add_f32 v[128:129], v[128:129], 0 op_sel_hi:[1,0]
	v_pk_mul_f32 v[124:125], v[124:125], v[36:37]
	v_pk_fma_f32 v[126:127], v[126:127], s[62:63], v[138:139] op_sel_hi:[1,0,1]
	v_pk_fma_f32 v[120:121], v[120:121], s[62:63], v[124:125] op_sel_hi:[1,0,1]
	v_lshlrev_b32_e32 v124, 16, v114
	v_and_b32_e32 v125, 0xffff0000, v114
	v_lshlrev_b32_e32 v114, 16, v115
	v_and_b32_e32 v115, 0xffff0000, v115
	v_pk_add_f32 v[114:115], v[114:115], 0 op_sel_hi:[1,0]
	v_pk_mul_f32 v[128:129], v[128:129], v[34:35]
	v_pk_mul_f32 v[114:115], v[114:115], v[64:65]
	v_pk_fma_f32 v[118:119], v[118:119], s[62:63], v[128:129] op_sel_hi:[1,0,1]
	v_pk_fma_f32 v[112:113], v[112:113], s[62:63], v[114:115] op_sel_hi:[1,0,1]
	v_lshlrev_b32_e32 v114, 16, v116
	v_and_b32_e32 v115, 0xffff0000, v116
	v_lshlrev_b32_e32 v116, 16, v117
	v_and_b32_e32 v117, 0xffff0000, v117
	v_pk_add_f32 v[114:115], v[114:115], 0 op_sel_hi:[1,0]
	v_pk_add_f32 v[116:117], v[116:117], 0 op_sel_hi:[1,0]
	v_pk_mul_f32 v[114:115], v[114:115], v[54:55]
	v_pk_add_f32 v[124:125], v[124:125], 0 op_sel_hi:[1,0]
	v_pk_mul_f32 v[116:117], v[116:117], v[56:57]
	v_pk_fma_f32 v[106:107], v[106:107], s[62:63], v[114:115] op_sel_hi:[1,0,1]
	v_add_f32_e32 v114, v126, v127
	v_add_f32_e32 v115, v122, v123
	v_pk_mul_f32 v[124:125], v[124:125], v[62:63]
	v_pk_fma_f32 v[108:109], v[108:109], s[62:63], v[116:117] op_sel_hi:[1,0,1]
	v_add_f32_e32 v114, v114, v115
	v_add_f32_e32 v115, v118, v119
	v_add_f32_e32 v116, v120, v121
	v_pk_fma_f32 v[110:111], v[110:111], s[62:63], v[124:125] op_sel_hi:[1,0,1]
	v_add_f32_e32 v114, 0, v114
	v_add_f32_e32 v115, v115, v116
	v_add_f32_e32 v114, v115, v114
	v_add_f32_e32 v115, v110, v111
	v_add_f32_e32 v116, v112, v113
	v_add_f32_e32 v115, v115, v116
	v_add_f32_e32 v114, v115, v114
	v_add_f32_e32 v115, v106, v107
	v_add_f32_e32 v116, v108, v109
	v_add_f32_e32 v115, v115, v116
	v_add_f32_e32 v114, v115, v114
	ds_swizzle_b32 v115, v114 offset:swizzle(SWAP,1)
	s_add_u32 s76, s76, 1
	s_addc_u32 s77, s77, 0
	s_waitcnt lgkmcnt(0)
	v_add_f32_e32 v114, v114, v115
	ds_swizzle_b32 v115, v114 offset:swizzle(SWAP,2)
	s_waitcnt lgkmcnt(0)
	v_add_f32_e32 v114, v114, v115
	ds_swizzle_b32 v115, v114 offset:swizzle(SWAP,4)
	s_waitcnt lgkmcnt(0)
	v_add_f32_e32 v114, v114, v115
	ds_swizzle_b32 v115, v114 offset:swizzle(SWAP,8)
	s_waitcnt lgkmcnt(0)
	v_add_f32_e32 v114, v114, v115
	ds_swizzle_b32 v115, v114 offset:swizzle(SWAP,16)
	s_waitcnt lgkmcnt(0)
	v_add_f32_e32 v114, v114, v115
	v_mov_b32_e32 v115, v114
	s_nop 1
	v_permlane32_swap_b32_e32 v114, v115
	v_add_f32_e32 v114, v114, v115
	v_fmac_f32_e32 v123, 0xba800000, v114
	v_fmac_f32_e32 v127, 0xba800000, v114
	v_fmamk_f32 v122, v114, 0xba800000, v122
	v_fmamk_f32 v126, v114, 0xba800000, v126
	v_mul_f32_e32 v115, v127, v127
	v_mul_f32_e32 v116, v123, v123
	v_fmac_f32_e32 v115, v126, v126
	v_fmac_f32_e32 v116, v122, v122
	v_fmac_f32_e32 v121, 0xba800000, v114
	v_fmac_f32_e32 v119, 0xba800000, v114
	v_add_f32_e32 v115, v115, v116
	v_fmamk_f32 v120, v114, 0xba800000, v120
	v_fmamk_f32 v118, v114, 0xba800000, v118
	v_mul_f32_e32 v116, v119, v119
	v_mul_f32_e32 v117, v121, v121
	v_fmac_f32_e32 v116, v118, v118
	v_fmac_f32_e32 v117, v120, v120
	v_add_f32_e32 v116, v116, v117
	v_fmac_f32_e32 v113, 0xba800000, v114
	v_fmac_f32_e32 v111, 0xba800000, v114
	v_add_f32_e32 v115, v115, v116
	v_fmamk_f32 v112, v114, 0xba800000, v112
	v_fmamk_f32 v110, v114, 0xba800000, v110
	v_mul_f32_e32 v116, v111, v111
	v_mul_f32_e32 v117, v113, v113
	v_fmac_f32_e32 v116, v110, v110
	v_fmac_f32_e32 v117, v112, v112
	v_add_f32_e32 v116, v116, v117
	v_fmac_f32_e32 v109, 0xba800000, v114
	v_fmac_f32_e32 v107, 0xba800000, v114
	v_add_f32_e32 v115, v116, v115
	v_fmamk_f32 v108, v114, 0xba800000, v108
	v_fmamk_f32 v106, v114, 0xba800000, v106
	v_mul_f32_e32 v114, v107, v107
	v_mul_f32_e32 v116, v109, v109
	v_fmac_f32_e32 v114, v106, v106
	v_fmac_f32_e32 v116, v108, v108
	v_add_f32_e32 v114, v114, v116
	v_add_f32_e32 v114, v114, v115
	ds_swizzle_b32 v115, v114 offset:swizzle(SWAP,1)
	s_waitcnt lgkmcnt(0)
; __device__ __forceinline__ unsigned pk2(float lo, float hi) { return f2bf(lo) | (f2bf(hi) << 16); }
; __device__ __forceinline__ unsigned cvt_fp8x4(float a, float b, float c, float d) { int w = __builtin_amdgcn_cvt_pk_fp8_f32(a, b, 0, false); w = __builtin_amdgcn_cvt_pk_fp8_f32(c, d, w, true); return (unsigned)w; }
; template <int MODE, bool FIRSTX>
; __device__ __forceinline__ void row_pass(Frame& F, int layer, bool final_out, int row0) {
;     ...
;             const float rstd = 1.0f / sqrtf(wave_sum(qq) * (1.0f / DM) + LN_EPS);
; #pragma unroll
;             for (int q = 0; q < 4; ++q) v[q] = v[q] * rstd * lg[q] + lb[q];
;             if (final_out) { if (row >= NCTX) {
; #pragma unroll
;                 for (int q = 0; q < 4; ++q) *(f32x4*)(F.out + (size_t)(row - NCTX) * DM + RP_COL(q)) = v[q]; } }
;             else {
; #pragma unroll
;                 for (int j = 0; j < 2; ++j) { u32x4 w; w.x = pk2(v[2 * j][0], v[2 * j][1]); w.y = pk2(v[2 * j][2], v[2 * j][3]); w.z = pk2(v[2 * j + 1][0], v[2 * j + 1][1]); w.w = pk2(v[2 * j + 1][2], v[2 * j + 1][3]);
;                     *(u32x4*)(X + (size_t)row * DM + lc + 512 * j) = w; } }
;         }
;         if (!final_out) {
; #pragma unroll
;             for (int j = 0; j < 2; ++j) { const f32x4 h0 = v[2 * j] * (sc[2 * j] + 1.0f) + sh[2 * j], h1 = v[2 * j + 1] * (sc[2 * j + 1] + 1.0f) + sh[2 * j + 1];
;                 if (MODE == 1 || (nlayer % 3) == 2) { u32x4 w; w.x = pk2(h0[0], h0[1]); w.y = pk2(h0[2], h0[3]); w.z = pk2(h1[0], h1[1]); w.w = pk2(h1[2], h1[3]);
;                     *(u32x4*)(H + (size_t)row * DM + lc + 512 * j) = w; }
;                 if (MODE == 1 || (nlayer % 3) != 2) {                                u32x2 w8; w8.x = cvt_fp8x4(h0[0], h0[1], h0[2], h0[3]); w8.y = cvt_fp8x4(h1[0], h1[1], h1[2], h1[3]); *(u32x2*)(F.ws + WS_H8 + (size_t)row * DM + lc + 512 * j) = w8; } }
	v_add_f32_e32 v114, v114, v115
	ds_swizzle_b32 v115, v114 offset:swizzle(SWAP,2)
	s_waitcnt lgkmcnt(0)
	v_add_f32_e32 v114, v114, v115
	ds_swizzle_b32 v115, v114 offset:swizzle(SWAP,4)
	s_waitcnt lgkmcnt(0)
	v_add_f32_e32 v114, v114, v115
	ds_swizzle_b32 v115, v114 offset:swizzle(SWAP,8)
	s_waitcnt lgkmcnt(0)
	v_add_f32_e32 v114, v114, v115
	ds_swizzle_b32 v115, v114 offset:swizzle(SWAP,16)
	s_waitcnt lgkmcnt(0)
	v_add_f32_e32 v114, v114, v115
	v_mov_b32_e32 v115, v114
	s_nop 1
	v_permlane32_swap_b32_e32 v114, v115
	v_add_f32_e32 v114, v114, v115
	v_fmamk_f32 v114, v114, 0x3a800000, v188
	v_mul_f32_e32 v115, 0x4f800000, v114
	v_cmp_gt_f32_e32 vcc, s31, v114
	s_nop 1
	v_cndmask_b32_e32 v114, v114, v115, vcc
	v_sqrt_f32_e32 v115, v114
	s_nop 0
	v_add_u32_e32 v116, -1, v115
	v_fma_f32 v117, -v116, v115, v114
	v_cmp_ge_f32_e64 s[2:3], 0, v117
	v_add_u32_e32 v117, 1, v115
	s_nop 0
	v_cndmask_b32_e64 v116, v115, v116, s[2:3]
	v_fma_f32 v115, -v117, v115, v114
	v_cmp_lt_f32_e64 s[2:3], 0, v115
	s_nop 1
	v_cndmask_b32_e64 v115, v116, v117, s[2:3]
	v_mul_f32_e32 v116, 0x37800000, v115
	v_cndmask_b32_e32 v115, v115, v116, vcc
	v_cmp_class_f32_e32 vcc, v114, v189
	s_nop 1
	v_cndmask_b32_e32 v114, v115, v114, vcc
	v_div_scale_f32 v115, s[0:1], v114, v114, 1.0
	v_rcp_f32_e32 v116, v115
	s_add_i32 s0, s4, s76
	s_add_u32 s60, s60, 0x1000
	s_addc_u32 s61, s61, 0
	v_fma_f32 v117, -v115, v116, 1.0
	v_fmac_f32_e32 v116, v117, v116
	v_div_scale_f32 v117, vcc, 1.0, v114, 1.0
	v_mul_f32_e32 v124, v117, v116
	v_fma_f32 v125, -v115, v124, v117
	v_fmac_f32_e32 v124, v125, v116
	v_fma_f32 v115, -v115, v124, v117
	v_div_fmas_f32 v115, v115, v116, v124
	v_div_fixup_f32 v114, v115, v114, 1.0
	v_pk_mul_f32 v[116:117], v[126:127], v[114:115] op_sel_hi:[1,0]
	v_pk_mul_f32 v[106:107], v[106:107], v[114:115] op_sel_hi:[1,0]
	v_pk_fma_f32 v[116:117], v[2:3], v[116:117], v[6:7]
	v_pk_mul_f32 v[122:123], v[122:123], v[114:115] op_sel_hi:[1,0]
	v_pk_mul_f32 v[118:119], v[118:119], v[114:115] op_sel_hi:[1,0]
	v_pk_mul_f32 v[120:121], v[120:121], v[114:115] op_sel_hi:[1,0]
	v_pk_mul_f32 v[110:111], v[110:111], v[114:115] op_sel_hi:[1,0]
	v_pk_mul_f32 v[112:113], v[112:113], v[114:115] op_sel_hi:[1,0]
	v_pk_mul_f32 v[108:109], v[108:109], v[114:115] op_sel_hi:[1,0]
	v_pk_fma_f32 v[114:115], v[26:27], v[106:107], v[30:31]
	v_bfe_u32 v106, v116, 16, 1
	v_add3_u32 v106, v116, v106, s43
	v_bfe_u32 v107, v117, 16, 1
	v_pk_fma_f32 v[122:123], v[4:5], v[122:123], v[8:9]
	v_lshrrev_b32_e32 v106, 16, v106
	v_add3_u32 v107, v117, v107, s43
	v_and_or_b32 v106, v107, s33, v106
	v_bfe_u32 v107, v122, 16, 1
	v_pk_fma_f32 v[124:125], v[28:29], v[108:109], v[32:33]
	v_add3_u32 v107, v122, v107, s43
	v_bfe_u32 v108, v123, 16, 1
	v_pk_fma_f32 v[118:119], v[10:11], v[118:119], v[14:15]
	v_lshrrev_b32_e32 v107, 16, v107
	v_add3_u32 v108, v123, v108, s43
	v_and_or_b32 v107, v108, s33, v107
	v_bfe_u32 v108, v118, 16, 1
	v_add3_u32 v108, v118, v108, s43
	v_bfe_u32 v109, v119, 16, 1
	v_pk_fma_f32 v[120:121], v[12:13], v[120:121], v[16:17]
	v_lshrrev_b32_e32 v108, 16, v108
	v_add3_u32 v109, v119, v109, s43
	v_and_or_b32 v108, v109, s33, v108
	v_bfe_u32 v109, v120, 16, 1
	v_add3_u32 v109, v120, v109, s43
	v_bfe_u32 v128, v121, 16, 1
	v_lshl_add_u64 v[126:127], s[74:75], 0, v[132:133]
	v_lshrrev_b32_e32 v109, 16, v109
	v_add3_u32 v128, v121, v128, s43
	v_and_or_b32 v109, v128, s33, v109
	v_add_co_u32_e32 v128, vcc, s39, v126
	v_pk_fma_f32 v[110:111], v[18:19], v[110:111], v[22:23]
	s_nop 0
	v_addc_co_u32_e32 v129, vcc, 0, v127, vcc
	global_store_dwordx4 v[128:129], v[106:109], off
	v_pk_fma_f32 v[112:113], v[20:21], v[112:113], v[24:25]
	v_bfe_u32 v137, v125, 16, 1
	v_bfe_u32 v106, v110, 16, 1
	v_add3_u32 v106, v110, v106, s43
	v_bfe_u32 v107, v111, 16, 1
	v_lshrrev_b32_e32 v106, 16, v106
	v_add3_u32 v107, v111, v107, s43
	v_and_or_b32 v106, v107, s33, v106
	v_bfe_u32 v107, v112, 16, 1
	v_add3_u32 v107, v112, v107, s43
	v_bfe_u32 v108, v113, 16, 1
	v_lshrrev_b32_e32 v107, 16, v107
	v_add3_u32 v108, v113, v108, s43
	v_and_or_b32 v107, v108, s33, v107
	v_bfe_u32 v108, v114, 16, 1
	v_add3_u32 v108, v114, v108, s43
	v_bfe_u32 v109, v115, 16, 1
	v_lshrrev_b32_e32 v108, 16, v108
	v_add3_u32 v109, v115, v109, s43
	v_and_or_b32 v108, v109, s33, v108
	v_bfe_u32 v109, v124, 16, 1
	v_add3_u32 v109, v124, v109, s43
	v_lshrrev_b32_e32 v109, 16, v109
	v_add3_u32 v137, v125, v137, s43
	v_and_or_b32 v109, v137, s33, v109
	global_store_dwordx4 v[128:129], v[106:109], off offset:1024
	v_lshl_add_u64 v[132:133], v[132:133], 0, s[50:51]
	s_cmp_ge_i32 s0, s11
	v_pk_add_f32 v[106:107], v[60:61], 1.0 op_sel_hi:[1,0]
	v_pk_add_f32 v[108:109], v[58:59], 1.0 op_sel_hi:[1,0]
	v_pk_fma_f32 v[122:123], v[106:107], v[122:123], v[48:49]
	v_pk_fma_f32 v[116:117], v[108:109], v[116:117], v[46:47]
	v_pk_add_f32 v[106:107], v[52:53], 1.0 op_sel_hi:[1,0]
	v_pk_add_f32 v[108:109], v[50:51], 1.0 op_sel_hi:[1,0]
	v_pk_fma_f32 v[120:121], v[106:107], v[120:121], v[44:45]
	v_and_b32_sdwa v107, v116, v185 dst_sel:DWORD dst_unused:UNUSED_PAD src0_sel:WORD_1 src1_sel:DWORD
	v_pk_fma_f32 v[118:119], v[108:109], v[118:119], v[42:43]
; __device__ __forceinline__ unsigned pk2(float lo, float hi) { return f2bf(lo) | (f2bf(hi) << 16); }
; __device__ __forceinline__ unsigned cvt_fp8x4(float a, float b, float c, float d) { int w = __builtin_amdgcn_cvt_pk_fp8_f32(a, b, 0, false); w = __builtin_amdgcn_cvt_pk_fp8_f32(c, d, w, true); return (unsigned)w; }
; template <int MODE, bool FIRSTX>
; __device__ __forceinline__ void row_pass(Frame& F, int layer, bool final_out, int row0) {
;     ...
;         if (!final_out) {
; #pragma unroll
;             for (int j = 0; j < 2; ++j) { const f32x4 h0 = v[2 * j] * (sc[2 * j] + 1.0f) + sh[2 * j], h1 = v[2 * j + 1] * (sc[2 * j + 1] + 1.0f) + sh[2 * j + 1];
;                 if (MODE == 1 || (nlayer % 3) == 2) { u32x4 w; w.x = pk2(h0[0], h0[1]); w.y = pk2(h0[2], h0[3]); w.z = pk2(h1[0], h1[1]); w.w = pk2(h1[2], h1[3]);
;                     *(u32x4*)(H + (size_t)row * DM + lc + 512 * j) = w; }
;                 if (MODE == 1 || (nlayer % 3) != 2) {                                u32x2 w8; w8.x = cvt_fp8x4(h0[0], h0[1], h0[2], h0[3]); w8.y = cvt_fp8x4(h1[0], h1[1], h1[2], h1[3]); *(u32x2*)(F.ws + WS_H8 + (size_t)row * DM + lc + 512 * j) = w8; } }
;         }
; #pragma unroll
;         for (int q = 0; q < 4; ++q) xf[q] = xfn[q];
; #pragma unroll
;         for (int j = 0; j < 2; ++j) { xb[j] = xbn[j];
; #pragma unroll
;             for (int k = 0; k < (NY ? NY : 1); ++k) yb[k][j] = ybn[k][j]; }
	v_add3_u32 v108, v116, v107, s43
	v_and_b32_sdwa v107, v123, v185 dst_sel:DWORD dst_unused:UNUSED_PAD src0_sel:WORD_1 src1_sel:DWORD
	v_and_b32_sdwa v109, v117, v185 dst_sel:DWORD dst_unused:UNUSED_PAD src0_sel:WORD_1 src1_sel:DWORD
	v_and_b32_sdwa v106, v122, v185 dst_sel:DWORD dst_unused:UNUSED_PAD src0_sel:WORD_1 src1_sel:DWORD
	v_add3_u32 v107, v123, v107, s43
	v_add3_u32 v109, v117, v109, s43
	v_add3_u32 v106, v122, v106, s43
	v_and_b32_e32 v107, 0xffff0000, v107
	v_and_b32_e32 v109, 0xffff0000, v109
	v_or_b32_sdwa v107, v107, v106 dst_sel:DWORD dst_unused:UNUSED_PAD src0_sel:DWORD src1_sel:WORD_1
	v_or_b32_sdwa v106, v109, v108 dst_sel:DWORD dst_unused:UNUSED_PAD src0_sel:DWORD src1_sel:WORD_1
	v_and_b32_sdwa v109, v118, v185 dst_sel:DWORD dst_unused:UNUSED_PAD src0_sel:WORD_1 src1_sel:DWORD
	v_add3_u32 v128, v118, v109, s43
	v_and_b32_sdwa v109, v121, v185 dst_sel:DWORD dst_unused:UNUSED_PAD src0_sel:WORD_1 src1_sel:DWORD
	v_and_b32_sdwa v129, v119, v185 dst_sel:DWORD dst_unused:UNUSED_PAD src0_sel:WORD_1 src1_sel:DWORD
	v_and_b32_sdwa v108, v120, v185 dst_sel:DWORD dst_unused:UNUSED_PAD src0_sel:WORD_1 src1_sel:DWORD
	v_add3_u32 v109, v121, v109, s43
	v_add3_u32 v129, v119, v129, s43
	v_add3_u32 v108, v120, v108, s43
	v_and_b32_e32 v109, 0xffff0000, v109
	v_and_b32_e32 v129, 0xffff0000, v129
	v_or_b32_sdwa v109, v109, v108 dst_sel:DWORD dst_unused:UNUSED_PAD src0_sel:DWORD src1_sel:WORD_1
	v_or_b32_sdwa v108, v129, v128 dst_sel:DWORD dst_unused:UNUSED_PAD src0_sel:DWORD src1_sel:WORD_1
	v_mov_b32_e32 v128, v1
	v_cvt_pk_fp8_f32 v128, v116, v117
	v_add_co_u32_e32 v116, vcc, s28, v126
	v_mov_b32_e32 v129, v1
	s_nop 0
	v_addc_co_u32_e32 v117, vcc, 0, v127, vcc
	v_cvt_pk_fp8_f32 v129, v118, v119
	global_store_dwordx4 v[116:117], v[106:109], off
	v_cvt_pk_fp8_f32 v128, v122, v123 op_sel:[0,0,1]
	v_cvt_pk_fp8_f32 v129, v120, v121 op_sel:[0,0,1]
	v_lshl_add_u64 v[106:107], s[74:75], 0, v[134:135]
	v_add_co_u32_e32 v118, vcc, s38, v106
	v_pk_add_f32 v[108:109], v[78:79], 1.0 op_sel_hi:[1,0]
	s_nop 0
	v_addc_co_u32_e32 v119, vcc, 0, v107, vcc
	v_pk_add_f32 v[106:107], v[80:81], 1.0 op_sel_hi:[1,0]
	v_pk_fma_f32 v[108:109], v[108:109], v[110:111], v[70:71]
	v_pk_fma_f32 v[112:113], v[106:107], v[112:113], v[72:73]
	v_pk_add_f32 v[106:107], v[76:77], 1.0 op_sel_hi:[1,0]
	v_pk_add_f32 v[110:111], v[74:75], 1.0 op_sel_hi:[1,0]
	v_pk_fma_f32 v[120:121], v[106:107], v[124:125], v[68:69]
	v_and_b32_sdwa v107, v108, v185 dst_sel:DWORD dst_unused:UNUSED_PAD src0_sel:WORD_1 src1_sel:DWORD
	v_pk_fma_f32 v[110:111], v[110:111], v[114:115], v[66:67]
	v_add3_u32 v114, v108, v107, s43
	v_and_b32_sdwa v107, v113, v185 dst_sel:DWORD dst_unused:UNUSED_PAD src0_sel:WORD_1 src1_sel:DWORD
	v_and_b32_sdwa v115, v109, v185 dst_sel:DWORD dst_unused:UNUSED_PAD src0_sel:WORD_1 src1_sel:DWORD
	v_and_b32_sdwa v106, v112, v185 dst_sel:DWORD dst_unused:UNUSED_PAD src0_sel:WORD_1 src1_sel:DWORD
	v_add3_u32 v107, v113, v107, s43
	v_add3_u32 v115, v109, v115, s43
	v_add3_u32 v106, v112, v106, s43
	v_and_b32_e32 v107, 0xffff0000, v107
	v_and_b32_e32 v115, 0xffff0000, v115
	v_or_b32_sdwa v107, v107, v106 dst_sel:DWORD dst_unused:UNUSED_PAD src0_sel:DWORD src1_sel:WORD_1
	v_or_b32_sdwa v106, v115, v114 dst_sel:DWORD dst_unused:UNUSED_PAD src0_sel:DWORD src1_sel:WORD_1
	v_and_b32_sdwa v114, v120, v185 dst_sel:DWORD dst_unused:UNUSED_PAD src0_sel:WORD_1 src1_sel:DWORD
	v_and_b32_sdwa v115, v110, v185 dst_sel:DWORD dst_unused:UNUSED_PAD src0_sel:WORD_1 src1_sel:DWORD
	v_add3_u32 v122, v110, v115, s43
	v_add3_u32 v123, v120, v114, s43
	v_and_b32_sdwa v114, v121, v185 dst_sel:DWORD dst_unused:UNUSED_PAD src0_sel:WORD_1 src1_sel:DWORD
	v_and_b32_sdwa v115, v111, v185 dst_sel:DWORD dst_unused:UNUSED_PAD src0_sel:WORD_1 src1_sel:DWORD
	v_add3_u32 v124, v121, v114, s43
	v_add3_u32 v125, v111, v115, s43
	v_mov_b32_e32 v114, v1
	v_mov_b32_e32 v115, v1
	v_cvt_pk_fp8_f32 v114, v108, v109
	v_cvt_pk_fp8_f32 v115, v110, v111
	v_and_b32_e32 v108, 0xffff0000, v124
	v_and_b32_e32 v110, 0xffff0000, v125
	v_cvt_pk_fp8_f32 v114, v112, v113 op_sel:[0,0,1]
	v_cvt_pk_fp8_f32 v115, v120, v121 op_sel:[0,0,1]
	v_or_b32_sdwa v109, v108, v123 dst_sel:DWORD dst_unused:UNUSED_PAD src0_sel:DWORD src1_sel:WORD_1
	v_or_b32_sdwa v108, v110, v122 dst_sel:DWORD dst_unused:UNUSED_PAD src0_sel:DWORD src1_sel:WORD_1
	global_store_dwordx2 v[118:119], v[128:129], off
	global_store_dwordx4 v[116:117], v[106:109], off offset:1024
	global_store_dwordx2 v[118:119], v[114:115], off offset:512
	s_waitcnt vmcnt(6)
	v_mov_b64_e32 v[112:113], v[96:97]
	v_mov_b64_e32 v[108:109], v[92:93]
	v_mov_b64_e32 v[120:121], v[84:85]
	v_mov_b64_e32 v[128:129], v[88:89]
	v_lshl_add_u64 v[134:135], v[134:135], 0, s[54:55]
	v_mov_b64_e32 v[106:107], v[90:91]
	v_mov_b64_e32 v[110:111], v[94:95]
	v_mov_b64_e32 v[118:119], v[82:83]
	v_mov_b64_e32 v[126:127], v[86:87]
	v_mov_b32_e32 v122, v98
	v_mov_b32_e32 v123, v99
	v_mov_b32_e32 v124, v100
	v_mov_b32_e32 v125, v101
	v_mov_b32_e32 v114, v102
	v_mov_b32_e32 v115, v103
	v_mov_b32_e32 v116, v104
	v_mov_b32_e32 v117, v105
	s_cbranch_scc1 .LBB0_777
